# EpiM2: per-row slot (list) loads issued one unit ahead into dedicated VGPRs; the epilogue's per-row vmcnt(0) waits (which serialised on the previous row's store) and the unit-start vmcnt(0) drain remo
# speedup vs baseline: 1.0170x; 1.0014x over previous
; #define GAS __attribute__((address_space(1)))
; DI int rfl(int v) { return __builtin_amdgcn_readfirstlane(v); }
; #define PG8_STAGE(bufoff, gbase, voff) do { _Pragma("unroll") for (int _i = 0; _i < 2; ++_i) \
;         __builtin_amdgcn_global_load_lds((const unsigned*)((const char*)(gbase) + (voff)[_i]), (LAS unsigned*)(lds + (bufoff) + ldsw + _i * 8192), 16, 0, 0); } while (0)
; #define PG8_WAIT_V(n) asm volatile("s_waitcnt vmcnt(" #n ")" ::: "memory")
; #define PG8_BAR __builtin_amdgcn_s_barrier()
; template <class Epi, class Sched, bool F8 = false>
; DI void gemm_phase(LAS unsigned char* lds, const int K, const Sched& S, const Epi& E) {
;     ...
;     unsigned oA[2][2]; S.a_off(cur, tid, oA);
;     const char* cA = S.a_base(cur); const char* cB = S.b_base(cur);
;     PG8_STAGE(PG8_SB(0, 0), cB, voffB); PG8_STAGE(PG8_SB(0, 1), cB + hstep, voffB); PG8_STAGE(PG8_SA(0, 0), cA, oA[0]); PG8_STAGE(PG8_SA(0, 1), cA, oA[1]);
;     if (wr == 1) PG8_BAR;
;     PG8_WAIT_V(2); PG8_BAR;
;     PG8_STAGE(PG8_SB(1, 0), cB + kstep, voffB); PG8_STAGE(PG8_SA(1, 0), cA + kstep, oA[0]); PG8_STAGE(PG8_SB(1, 1), cB + hstep + kstep, voffB);
;     PG8_WAIT_V(6); PG8_BAR;
;     DI void operator()(const f32x4 (&acc)[2][2][4][2], const Unit& u, int wr, int wc, int fr, int fq) const {
;     ...
;         const int lrow0 = wr * 64 + fr, col0 = u.pn * 256 + wc * 32 + 8 * fq; const int lt = u.pm - rfl(pre[u.e]);
;         const int* lp = list + (size_t)u.e * T + 256 * lt;
;         int slotv[8];
; #pragma unroll
;         for (int q = 0; q < 8; ++q) { const int r = lrow0 + (q >> 2) * 128 + (q & 3) * 16; slotv[q] = ((const GAS int*)lp)[r < u.nv ? r : 0]; }
.LBB0_1633:
	s_add_u32 s56, s46, 0x313c0000
	s_addc_u32 s57, s47, 0
	s_add_u32 s2, s46, 0xffc0000
	v_bfe_u32 v5, v14, 4, 2
	v_writelane_b32 v254, s2, 38
	v_writelane_b32 v255, s46, 48
	s_addc_u32 s2, s47, 0
	v_and_b32_e32 v1, 15, v14
	v_lshlrev_b32_e32 v19, 4, v5
	v_lshlrev_b32_e32 v14, 2, v14
	v_writelane_b32 v254, s2, 34
	s_lshl_b32 s2, s1, 6
	v_lshl_or_b32 v19, v1, 6, v19
	s_lshl_b32 s1, s1, 13
	v_and_b32_e32 v14, 32, v14
	v_bitop3_b32 v20, v19, s1, v14 bitop3:0xde
	s_lshl_b32 s1, s0, 5
	s_add_i32 s96, s38, 0x18000
	s_and_b32 s95, s1, 0x60
	s_add_i32 s5, s96, s6
	s_lshl_b32 s1, s95, 7
	v_lshl_add_u64 v[10:11], v[10:11], 0, s[24:25]
	s_mov_b32 m0, s5
	s_add_i32 s97, s5, 0x2000
	s_add_i32 s80, s88, 0x8000
	s_add_i32 s81, s88, 0xa000
	global_load_lds_dwordx4 v[10:11], off
	v_lshl_add_u64 v[8:9], v[8:9], 0, s[24:25]
	s_mov_b32 m0, s97
	s_add_u32 s8, s50, 0x20080
	global_load_lds_dwordx4 v[8:9], off
	v_lshl_add_u64 v[6:7], v[6:7], 0, s[24:25]
	s_mov_b32 m0, s80
	s_addc_u32 s9, s51, 0
	s_add_i32 s4, s38, 0x1c000
	global_load_lds_dwordx4 v[6:7], off
	v_lshl_add_u64 v[6:7], v[12:13], 0, s[24:25]
	s_mov_b32 m0, s81
	s_add_i32 s79, s4, s6
	global_load_lds_dwordx4 v[6:7], off
	v_lshl_add_u64 v[6:7], s[8:9], 0, v[2:3]
	s_mov_b32 m0, s79
	s_add_i32 s78, s79, 0x2000
	global_load_lds_dwordx4 v[6:7], off
	v_lshl_add_u64 v[6:7], s[8:9], 0, v[166:167]
	s_mov_b32 m0, s78
	s_cmp_lt_u32 s0, 4
	global_load_lds_dwordx4 v[6:7], off
	v_writelane_b32 v255, s47, 49
	s_cselect_b64 s[58:59], -1, 0
	s_add_i32 s0, s38, 0x27f04
	v_writelane_b32 v255, s0, 36
	s_add_i32 s0, s38, 0x27f08
	v_writelane_b32 v255, s0, 16
	s_add_i32 s0, s38, 0x27f0c
	v_writelane_b32 v255, s0, 20
	s_add_i32 s0, s38, 0x27f10
	v_writelane_b32 v254, s2, 36
	v_writelane_b32 v255, s0, 26
	s_add_i32 s0, s38, 0x27f14
	v_writelane_b32 v254, s0, 40
	s_add_i32 s0, s38, 0x27f18
	v_writelane_b32 v254, s0, 57
	s_add_i32 s0, s38, 0x27f1c
	v_writelane_b32 v255, s0, 18
	s_add_i32 s0, s38, 0x27f20
	v_writelane_b32 v255, s0, 0
	s_add_i32 s0, s38, 0x27f24
	v_writelane_b32 v255, s0, 4
	s_add_i32 s0, s38, 0x27f28
	v_writelane_b32 v255, s0, 8
	s_add_i32 s0, s38, 0x27f2c
	v_writelane_b32 v255, s0, 14
	s_add_i32 s0, s38, 0x27f30
	v_writelane_b32 v255, s0, 28
	s_add_i32 s0, s38, 0x27f34
	v_writelane_b32 v255, s0, 10
	s_add_i32 s0, s38, 0x27f38
	s_waitcnt vmcnt(8)
	s_barrier
	s_waitcnt vmcnt(6)
	v_writelane_b32 v255, s0, 22
	s_add_i32 s0, s38, 0x27f3c
	v_writelane_b32 v255, s0, 24
	s_mov_b32 s0, 0x20000
	v_bitop3_b32 v177, v19, s1, v14 bitop3:0xde
	v_add3_u32 v176, v15, v17, s0
	v_add3_u32 v178, v16, v18, s0
	s_mov_b32 s92, 0
	v_add_u32_e32 v179, s38, v20
	s_mov_b32 s2, s17
	s_barrier
	s_lshl_b32 s98, s44, 2
	s_add_i32 s98, s39, s98
	v_mov_b32_e32 v203, s98
	ds_read_b32 v203, v203
	v_readlane_b32 s100, v254, 38
	v_readlane_b32 s101, v254, 34
	s_lshl_b32 s98, s44, 18
	s_add_u32 s100, s100, s98
	s_addc_u32 s101, s101, 0
	s_waitcnt lgkmcnt(0)
	v_readfirstlane_b32 s98, v203
	s_sub_i32 s98, s42, s98
	s_lshl_b32 s98, s98, 10
	s_ashr_i32 s99, s98, 31
	s_add_u32 s100, s100, s98
	s_addc_u32 s101, s101, s99
	v_readlane_b32 s98, v254, 36
	s_nop 1
	v_add_u32_e32 v203, s98, v1
	v_add_u32_e32 v206, 0x10, v203
	v_add_u32_e32 v235, 0x20, v203
	v_add_u32_e32 v244, 0x30, v203
	v_add_u32_e32 v245, 0x80, v203
	v_add_u32_e32 v246, 0x90, v203
	v_add_u32_e32 v247, 0xa0, v203
	v_add_u32_e32 v249, 0xb0, v203
	v_cmp_gt_i32_e64 s[98:99], s93, v206
	s_nop 1
	v_cndmask_b32_e64 v206, 0, v206, s[98:99]
	v_lshlrev_b32_e32 v206, 2, v206
	global_load_dword v206, v206, s[100:101]
	v_cmp_gt_i32_e64 s[98:99], s93, v235
	s_nop 1
	v_cndmask_b32_e64 v235, 0, v235, s[98:99]
	v_lshlrev_b32_e32 v235, 2, v235
	global_load_dword v235, v235, s[100:101]
	v_cmp_gt_i32_e64 s[98:99], s93, v244
	s_nop 1
	v_cndmask_b32_e64 v244, 0, v244, s[98:99]
	v_lshlrev_b32_e32 v244, 2, v244
	global_load_dword v244, v244, s[100:101]
	v_cmp_gt_i32_e64 s[98:99], s93, v245
	s_nop 1
	v_cndmask_b32_e64 v245, 0, v245, s[98:99]
	v_lshlrev_b32_e32 v245, 2, v245
	global_load_dword v245, v245, s[100:101]
	v_cmp_gt_i32_e64 s[98:99], s93, v246
	s_nop 1
	v_cndmask_b32_e64 v246, 0, v246, s[98:99]
	v_lshlrev_b32_e32 v246, 2, v246
	global_load_dword v246, v246, s[100:101]
	v_cmp_gt_i32_e64 s[98:99], s93, v247
	s_nop 1
	v_cndmask_b32_e64 v247, 0, v247, s[98:99]
	v_lshlrev_b32_e32 v247, 2, v247
	global_load_dword v247, v247, s[100:101]
	v_cmp_gt_i32_e64 s[98:99], s93, v249
	s_nop 1
	v_cndmask_b32_e64 v249, 0, v249, s[98:99]
	v_lshlrev_b32_e32 v249, 2, v249
	global_load_dword v249, v249, s[100:101]
	v_cmp_gt_i32_e64 s[98:99], s93, v203
	s_nop 1
	v_cndmask_b32_e64 v203, 0, v203, s[98:99]
	v_lshlrev_b32_e32 v203, 2, v203
	global_load_dword v203, v203, s[100:101]
	s_branch .LBB0_1636

; #define PG8_STAGE(bufoff, gbase, voff) do { _Pragma("unroll") for (int _i = 0; _i < 2; ++_i) \
;         __builtin_amdgcn_global_load_lds((const unsigned*)((const char*)(gbase) + (voff)[_i]), (LAS unsigned*)(lds + (bufoff) + ldsw + _i * 8192), 16, 0, 0); } while (0)
; #define PG8_LDA(dst, b, h) do { if constexpr (F8) { _Pragma("unroll") for (int m = 0; m < 4; ++m) dst##8[m] = PG8_LD8(lds + PG8_SA(b, h) + aoff + m * 2048); } else { \
;         _Pragma("unroll") for (int m = 0; m < 4; ++m) _Pragma("unroll") for (int k = 0; k < 2; ++k) dst[m][k] = *(const LAS bf16x8*)(lds + PG8_SA(b, h) + aoff + m * 2048 + k * 1024); } } while (0)
; #define PG8_LDB(dst, b, h) do { if constexpr (F8) { _Pragma("unroll") for (int n = 0; n < 2; ++n) dst##8[n] = PG8_LD8(lds + PG8_SB(b, h) + boff + n * 2048); } else { \
;         _Pragma("unroll") for (int n = 0; n < 2; ++n) _Pragma("unroll") for (int k = 0; k < 2; ++k) dst[n][k] = *(const LAS bf16x8*)(lds + PG8_SB(b, h) + boff + n * 2048 + k * 1024); } } while (0)
; #define PG8_MMA0(ai, bj, At, Bt) do { __builtin_amdgcn_s_setprio(1); _Pragma("unroll") for (int m = 0; m < 4; ++m) _Pragma("unroll") for (int n = 0; n < 2; ++n) \
;         asm volatile("v_mfma_f32_16x16x128_f8f6f4 %0, %1, %2, 0" : "=&v"(acc[ai][bj][m][n]) : "v"(Bt##8[n]), "v"(At##8[m])); __builtin_amdgcn_s_setprio(0); } while (0)
; #define PG8_WAIT_L(n) asm volatile("s_waitcnt lgkmcnt(" #n ")" ::: "memory")
; #define PG8_BAR __builtin_amdgcn_s_barrier()
; #define PG8_SCHED __builtin_amdgcn_sched_barrier(0)
; template <class Epi, class Sched, bool F8 = false>
; DI void gemm_phase(LAS unsigned char* lds, const int K, const Sched& S, const Epi& E) {
;     ...
;             PG8_LDB(B0, 0, 0); PG8_LDB(B1, 0, 1); PG8_SCHED; PG8_LDA(At, 0, 0); PG8_STAGE(PG8_SA(1, 1), a1, oA[1]);
;             if (last && has_next) S.a_off(nxt, tid, oA);
;             PG8_WAIT_VX(sxe); PG8_WAIT_L(0); PG8_BAR; if (F8 && t == 0) { PG8_MMA0(0, 0, At, B0); PG8_MMA0(0, 1, At, B1); } else { PG8_MMA(0, 0, At, B0); PG8_MMA(0, 1, At, B1); } PG8_BAR; PG8_SCHED;
;             PG8_LDA(At, 0, 1); PG8_STAGE(PG8_SB(0, 0), b2, voffB); PG8_STAGE(PG8_SB(0, 1), b2 + hstep, voffB); PG8_STAGE(PG8_SA(0, 0), a2, oA[0]);
;             PG8_WAIT_VX(sxe); PG8_WAIT_L(0); PG8_BAR; if (F8 && t == 0) { PG8_MMA0(1, 0, At, B0); PG8_MMA0(1, 1, At, B1); } else { PG8_MMA(1, 0, At, B0); PG8_MMA(1, 1, At, B1); } PG8_BAR; PG8_SCHED;
.LBB0_1640:
	v_add_u32_e32 v188, s82, v177
	v_add_u32_e32 v189, s85, v177
	ds_read_b128 v[6:9], v188
	s_nop 0
	ds_read_b128 v[10:13], v188 offset:1024
	ds_read_b128 v[14:17], v188 offset:2048
	ds_read_b128 v[18:21], v188 offset:3072
	ds_read_b128 v[22:25], v189
	ds_read_b128 v[26:29], v189 offset:1024
	ds_read_b128 v[30:33], v189 offset:2048
	ds_read_b128 v[34:37], v189 offset:3072
	s_ashr_i32 s17, s16, 31
	s_lshl_b64 s[0:1], s[16:17], 18
	s_add_u32 s0, s61, s0
	s_addc_u32 s1, s75, s1
	s_and_b64 s[6:7], s[46:47], exec
	s_cselect_b32 s17, s1, s49
	s_cselect_b32 s43, s0, s48
	v_mov_b32_e32 v171, v4
	v_lshl_add_u64 v[200:201], s[48:49], 0, v[170:171]
	s_add_i32 s45, s88, 0xc000
	v_mov_b32_e32 v175, v4
	v_lshl_add_u64 v[70:71], v[200:201], 0, s[24:25]
	s_mov_b32 m0, s45
	v_lshl_add_u64 v[220:221], s[48:49], 0, v[174:175]
	s_add_i32 s54, s88, 0xe000
	ds_read_b128 v[38:41], v179
	ds_read_b128 v[42:45], v179 offset:1024
	ds_read_b128 v[46:49], v179 offset:2048
	ds_read_b128 v[50:53], v179 offset:3072
	ds_read_b128 v[54:57], v179 offset:4096
	ds_read_b128 v[58:61], v179 offset:5120
	ds_read_b128 v[62:65], v179 offset:6144
	ds_read_b128 v[66:69], v179 offset:7168
	global_load_lds_dwordx4 v[70:71], off
	v_lshl_add_u64 v[70:71], v[220:221], 0, s[24:25]
	s_mov_b32 m0, s54
	s_nop 0
	global_load_lds_dwordx4 v[70:71], off
	s_waitcnt vmcnt(8)
	s_waitcnt lgkmcnt(0)
	s_barrier
	s_setprio 1
	s_waitcnt lgkmcnt(0)
	v_mfma_f32_16x16x128_f8f6f4 v[162:165], v[6:13], v[38:45], 0
	v_mfma_f32_16x16x128_f8f6f4 v[158:161], v[14:21], v[38:45], 0
	v_mfma_f32_16x16x128_f8f6f4 v[146:149], v[6:13], v[46:53], 0
	v_mfma_f32_16x16x128_f8f6f4 v[142:145], v[14:21], v[46:53], 0
	v_mfma_f32_16x16x128_f8f6f4 v[130:133], v[6:13], v[54:61], 0
	v_mfma_f32_16x16x128_f8f6f4 v[126:129], v[14:21], v[54:61], 0
	v_mfma_f32_16x16x128_f8f6f4 v[106:109], v[6:13], v[62:69], 0
	v_mfma_f32_16x16x128_f8f6f4 v[98:101], v[14:21], v[62:69], 0
	s_setprio 0
	s_setprio 1
	v_mfma_f32_16x16x128_f8f6f4 v[154:157], v[22:29], v[38:45], 0
	v_mfma_f32_16x16x128_f8f6f4 v[150:153], v[30:37], v[38:45], 0
	v_mfma_f32_16x16x128_f8f6f4 v[138:141], v[22:29], v[46:53], 0
	v_mfma_f32_16x16x128_f8f6f4 v[134:137], v[30:37], v[46:53], 0
	v_mfma_f32_16x16x128_f8f6f4 v[122:125], v[22:29], v[54:61], 0
	v_mfma_f32_16x16x128_f8f6f4 v[118:121], v[30:37], v[54:61], 0
	v_mfma_f32_16x16x128_f8f6f4 v[90:93], v[22:29], v[62:69], 0
	v_mfma_f32_16x16x128_f8f6f4 v[86:89], v[30:37], v[62:69], 0
	s_setprio 0
	s_barrier
	v_lshl_add_u64 v[180:181], s[50:51], 0, v[2:3]
	s_mov_b32 m0, s83
	v_lshl_add_u64 v[46:47], v[180:181], 0, s[28:29]
	v_lshl_add_u64 v[182:183], s[50:51], 0, v[166:167]
	s_add_u32 s6, s50, 0x20100
	ds_read_b128 v[38:41], v179 offset:16384
	ds_read_b128 v[42:45], v179 offset:17408
	ds_read_b128 v[54:57], v179 offset:18432
	ds_read_b128 v[58:61], v179 offset:19456
	ds_read_b128 v[190:193], v179 offset:20480
	ds_read_b128 v[194:197], v179 offset:21504
	ds_read_b128 v[212:215], v179 offset:22528
	ds_read_b128 v[216:219], v179 offset:23552
	global_load_lds_dwordx4 v[46:47], off
	v_lshl_add_u64 v[46:47], v[182:183], 0, s[28:29]
	s_mov_b32 m0, s84
	s_addc_u32 s7, s51, 0
	global_load_lds_dwordx4 v[46:47], off
	v_lshl_add_u64 v[46:47], s[6:7], 0, v[2:3]
	s_mov_b32 m0, s86
	v_lshl_add_u64 v[184:185], s[48:49], 0, v[168:169]
	global_load_lds_dwordx4 v[46:47], off
	v_lshl_add_u64 v[46:47], s[6:7], 0, v[166:167]
	s_mov_b32 m0, s87
	v_lshl_add_u64 v[186:187], s[48:49], 0, v[172:173]
	global_load_lds_dwordx4 v[46:47], off
	v_lshl_add_u64 v[46:47], v[184:185], 0, s[28:29]
	s_mov_b32 m0, s88
	s_nop 0
	global_load_lds_dwordx4 v[46:47], off
	v_lshl_add_u64 v[46:47], v[186:187], 0, s[28:29]
	s_mov_b32 m0, s89
	s_nop 0
	global_load_lds_dwordx4 v[46:47], off
	s_waitcnt vmcnt(8)
	s_waitcnt lgkmcnt(0)
	s_barrier
	s_setprio 1
	s_waitcnt lgkmcnt(0)
	v_mfma_f32_16x16x128_f8f6f4 v[114:117], v[6:13], v[38:45], 0
	v_mfma_f32_16x16x128_f8f6f4 v[110:113], v[14:21], v[38:45], 0
	v_mfma_f32_16x16x128_f8f6f4 v[82:85], v[6:13], v[54:61], 0
	v_mfma_f32_16x16x128_f8f6f4 v[78:81], v[14:21], v[54:61], 0
	v_mfma_f32_16x16x128_f8f6f4 v[66:69], v[6:13], v[190:197], 0
	v_mfma_f32_16x16x128_f8f6f4 v[62:65], v[14:21], v[190:197], 0
	v_mfma_f32_16x16x128_f8f6f4 v[50:53], v[6:13], v[212:219], 0
	v_mfma_f32_16x16x128_f8f6f4 v[46:49], v[14:21], v[212:219], 0
	s_setprio 0
	s_setprio 1
	v_mfma_f32_16x16x128_f8f6f4 v[102:105], v[22:29], v[38:45], 0
	v_mfma_f32_16x16x128_f8f6f4 v[94:97], v[30:37], v[38:45], 0
	v_mfma_f32_16x16x128_f8f6f4 v[74:77], v[22:29], v[54:61], 0
	v_mfma_f32_16x16x128_f8f6f4 v[70:73], v[30:37], v[54:61], 0
	v_mfma_f32_16x16x128_f8f6f4 v[58:61], v[22:29], v[190:197], 0
	v_mfma_f32_16x16x128_f8f6f4 v[54:57], v[30:37], v[190:197], 0
	v_mfma_f32_16x16x128_f8f6f4 v[42:45], v[22:29], v[212:219], 0
	v_mfma_f32_16x16x128_f8f6f4 v[38:41], v[30:37], v[212:219], 0
	s_setprio 0
	s_barrier
; #define PG8_STAGE(bufoff, gbase, voff) do { _Pragma("unroll") for (int _i = 0; _i < 2; ++_i) \
;         __builtin_amdgcn_global_load_lds((const unsigned*)((const char*)(gbase) + (voff)[_i]), (LAS unsigned*)(lds + (bufoff) + ldsw + _i * 8192), 16, 0, 0); } while (0)
; #define PG8_LDA(dst, b, h) do { if constexpr (F8) { _Pragma("unroll") for (int m = 0; m < 4; ++m) dst##8[m] = PG8_LD8(lds + PG8_SA(b, h) + aoff + m * 2048); } else { \
;         _Pragma("unroll") for (int m = 0; m < 4; ++m) _Pragma("unroll") for (int k = 0; k < 2; ++k) dst[m][k] = *(const LAS bf16x8*)(lds + PG8_SA(b, h) + aoff + m * 2048 + k * 1024); } } while (0)
; #define PG8_LDB(dst, b, h) do { if constexpr (F8) { _Pragma("unroll") for (int n = 0; n < 2; ++n) dst##8[n] = PG8_LD8(lds + PG8_SB(b, h) + boff + n * 2048); } else { \
;         _Pragma("unroll") for (int n = 0; n < 2; ++n) _Pragma("unroll") for (int k = 0; k < 2; ++k) dst[n][k] = *(const LAS bf16x8*)(lds + PG8_SB(b, h) + boff + n * 2048 + k * 1024); } } while (0)
; #define PG8_WAIT_V(n) asm volatile("s_waitcnt vmcnt(" #n ")" ::: "memory")
; #define PG8_WAIT_L(n) asm volatile("s_waitcnt lgkmcnt(" #n ")" ::: "memory")
; #define PG8_BAR __builtin_amdgcn_s_barrier()
; #define PG8_SCHED __builtin_amdgcn_sched_barrier(0)
; template <class Epi, class Sched, bool F8 = false>
; DI void gemm_phase(LAS unsigned char* lds, const int K, const Sched& S, const Epi& E) {
;     ...
;             PG8_LDB(B0, 1, 0); PG8_LDB(B1, 1, 1); PG8_SCHED; PG8_LDA(At, 1, 0); PG8_STAGE(PG8_SA(0, 1), a2, oA[1]);
;             PG8_WAIT_V(8); PG8_WAIT_L(0); PG8_BAR; PG8_MMA(0, 0, At, B0); PG8_MMA(0, 1, At, B1); PG8_BAR; PG8_SCHED;
;             PG8_LDA(At, 1, 1); PG8_STAGE(PG8_SB(1, 0), b3, voffB); PG8_STAGE(PG8_SB(1, 1), b3 + hstep, voffB); PG8_STAGE(PG8_SA(1, 0), a3, oA[0]);
;             PG8_WAIT_V(8); PG8_WAIT_L(0); PG8_BAR; PG8_MMA(1, 0, At, B0); PG8_MMA(1, 1, At, B1); PG8_BAR; PG8_SCHED;
	v_add_u32_e32 v190, s96, v177
	v_add_u32_e32 v191, s4, v177
	ds_read_b128 v[22:25], v190
	ds_read_b128 v[26:29], v190 offset:1024
	ds_read_b128 v[30:33], v190 offset:2048
	ds_read_b128 v[34:37], v190 offset:3072
	ds_read_b128 v[6:9], v191
	ds_read_b128 v[10:13], v191 offset:1024
	ds_read_b128 v[14:17], v191 offset:2048
	ds_read_b128 v[18:21], v191 offset:3072
	s_mov_b32 m0, s90
	v_lshl_add_u64 v[200:201], v[200:201], 0, s[28:29]
	ds_read_b128 v[192:195], v179 offset:32768
	ds_read_b128 v[196:199], v179 offset:33792
	ds_read_b128 v[212:215], v179 offset:34816
	ds_read_b128 v[216:219], v179 offset:35840
	ds_read_b128 v[226:229], v179 offset:36864
	ds_read_b128 v[230:233], v179 offset:37888
	ds_read_b128 v[236:239], v179 offset:38912
	ds_read_b128 v[240:243], v179 offset:39936
	global_load_lds_dwordx4 v[200:201], off
	v_lshl_add_u64 v[200:201], v[220:221], 0, s[28:29]
	s_mov_b32 m0, s91
	s_nop 0
	global_load_lds_dwordx4 v[200:201], off
	s_waitcnt vmcnt(8)
	s_waitcnt lgkmcnt(0)
	s_barrier
	s_setprio 1
	s_waitcnt lgkmcnt(0)
	v_mfma_f32_16x16x128_f8f6f4 v[162:165], v[22:29], v[192:199], v[162:165]
	v_mfma_f32_16x16x128_f8f6f4 v[158:161], v[30:37], v[192:199], v[158:161]
	v_mfma_f32_16x16x128_f8f6f4 v[146:149], v[22:29], v[212:219], v[146:149]
	v_mfma_f32_16x16x128_f8f6f4 v[142:145], v[30:37], v[212:219], v[142:145]
	v_mfma_f32_16x16x128_f8f6f4 v[130:133], v[22:29], v[226:233], v[130:133]
	v_mfma_f32_16x16x128_f8f6f4 v[126:129], v[30:37], v[226:233], v[126:129]
	v_mfma_f32_16x16x128_f8f6f4 v[106:109], v[22:29], v[236:243], v[106:109]
	v_mfma_f32_16x16x128_f8f6f4 v[98:101], v[30:37], v[236:243], v[98:101]
	s_setprio 0
	s_setprio 1
	v_mfma_f32_16x16x128_f8f6f4 v[154:157], v[6:13], v[192:199], v[154:157]
	v_mfma_f32_16x16x128_f8f6f4 v[150:153], v[14:21], v[192:199], v[150:153]
	v_mfma_f32_16x16x128_f8f6f4 v[138:141], v[6:13], v[212:219], v[138:141]
	v_mfma_f32_16x16x128_f8f6f4 v[134:137], v[14:21], v[212:219], v[134:137]
	v_mfma_f32_16x16x128_f8f6f4 v[122:125], v[6:13], v[226:233], v[122:125]
	v_mfma_f32_16x16x128_f8f6f4 v[118:121], v[14:21], v[226:233], v[118:121]
	v_mfma_f32_16x16x128_f8f6f4 v[90:93], v[6:13], v[236:243], v[90:93]
	v_mfma_f32_16x16x128_f8f6f4 v[86:89], v[14:21], v[236:243], v[86:89]
	s_setprio 0
	s_barrier
	s_mov_b32 m0, s5
	v_lshl_add_u64 v[180:181], v[180:181], 0, s[26:27]
	s_add_u32 s6, s50, 0x20180
	ds_read_b128 v[192:195], v179 offset:49152
	ds_read_b128 v[196:199], v179 offset:50176
	ds_read_b128 v[212:215], v179 offset:51200
	ds_read_b128 v[216:219], v179 offset:52224
	ds_read_b128 v[226:229], v179 offset:53248
	ds_read_b128 v[230:233], v179 offset:54272
	ds_read_b128 v[236:239], v179 offset:55296
	ds_read_b128 v[240:243], v179 offset:56320
	global_load_lds_dwordx4 v[180:181], off
	v_lshl_add_u64 v[180:181], v[182:183], 0, s[26:27]
	s_mov_b32 m0, s97
	s_addc_u32 s7, s51, 0
	global_load_lds_dwordx4 v[180:181], off
	v_lshl_add_u64 v[180:181], s[6:7], 0, v[2:3]
	s_mov_b32 m0, s79
	s_nop 0
	global_load_lds_dwordx4 v[180:181], off
	v_lshl_add_u64 v[180:181], s[6:7], 0, v[166:167]
	s_mov_b32 m0, s78
	s_nop 0
	global_load_lds_dwordx4 v[180:181], off
	v_lshl_add_u64 v[180:181], v[184:185], 0, s[26:27]
	s_mov_b32 m0, s80
	s_nop 0
	global_load_lds_dwordx4 v[180:181], off
	v_lshl_add_u64 v[180:181], v[186:187], 0, s[26:27]
	s_mov_b32 m0, s81
	s_nop 0
	global_load_lds_dwordx4 v[180:181], off
	s_waitcnt vmcnt(8)
	s_waitcnt lgkmcnt(0)
	s_barrier
	s_setprio 1
	s_waitcnt lgkmcnt(0)
	v_mfma_f32_16x16x128_f8f6f4 v[114:117], v[22:29], v[192:199], v[114:117]
	v_mfma_f32_16x16x128_f8f6f4 v[110:113], v[30:37], v[192:199], v[110:113]
	v_mfma_f32_16x16x128_f8f6f4 v[82:85], v[22:29], v[212:219], v[82:85]
	v_mfma_f32_16x16x128_f8f6f4 v[78:81], v[30:37], v[212:219], v[78:81]
	v_mfma_f32_16x16x128_f8f6f4 v[66:69], v[22:29], v[226:233], v[66:69]
	v_mfma_f32_16x16x128_f8f6f4 v[62:65], v[30:37], v[226:233], v[62:65]
	v_mfma_f32_16x16x128_f8f6f4 v[50:53], v[22:29], v[236:243], v[50:53]
	v_mfma_f32_16x16x128_f8f6f4 v[46:49], v[30:37], v[236:243], v[46:49]
	s_setprio 0
	s_setprio 1
	v_mfma_f32_16x16x128_f8f6f4 v[102:105], v[6:13], v[192:199], v[102:105]
	v_mfma_f32_16x16x128_f8f6f4 v[94:97], v[14:21], v[192:199], v[94:97]
	v_mfma_f32_16x16x128_f8f6f4 v[74:77], v[6:13], v[212:219], v[74:77]
	v_mfma_f32_16x16x128_f8f6f4 v[70:73], v[14:21], v[212:219], v[70:73]
	v_mfma_f32_16x16x128_f8f6f4 v[58:61], v[6:13], v[226:233], v[58:61]
	v_mfma_f32_16x16x128_f8f6f4 v[54:57], v[14:21], v[226:233], v[54:57]
	v_mfma_f32_16x16x128_f8f6f4 v[42:45], v[6:13], v[236:243], v[42:45]
	v_mfma_f32_16x16x128_f8f6f4 v[38:41], v[14:21], v[236:243], v[38:41]
	s_setprio 0
	s_barrier
	s_add_u32 s6, s50, 0x200
	s_addc_u32 s7, s51, 0
	s_add_u32 s48, s48, 0x180
	s_addc_u32 s49, s49, 0
	s_mov_b32 s55, 0

; #define GAS __attribute__((address_space(1)))
; DI int rfl(int v) { return __builtin_amdgcn_readfirstlane(v); }
; DI unsigned pk4_fp8(float a, float b, float c_, float d) { int w = 0; w = __builtin_amdgcn_cvt_pk_fp8_f32(clamp8(a), clamp8(b), w, false); w = __builtin_amdgcn_cvt_pk_fp8_f32(clamp8(c_), clamp8(d), w, true); return (unsigned)w; }
;     DI void operator()(const f32x4 (&acc)[2][2][4][2], const Unit& u, int wr, int wc, int fr, int fq) const {
;         asm volatile("" : "+v"(fr), "+v"(fq));
;         const int lrow0 = wr * 64 + fr, col0 = u.pn * 256 + wc * 32 + 8 * fq; const int lt = u.pm - rfl(pre[u.e]);
;         const int* lp = list + (size_t)u.e * T + 256 * lt;
;         int slotv[8];
; #pragma unroll
;         for (int q = 0; q < 8; ++q) { const int r = lrow0 + (q >> 2) * 128 + (q & 3) * 16; slotv[q] = ((const GAS int*)lp)[r < u.nv ? r : 0]; }
; #pragma unroll
;         for (int ai = 0; ai < 2; ++ai)
; #pragma unroll
;             for (int m = 0; m < 4; ++m) { const int r = lrow0 + ai * 128 + m * 16;
;                 if (r < u.nv) { const int slot = slotv[ai * 4 + m]; unsigned char* yp = ys + (size_t)slot * 1024 + col0;
;                     u32x2 o[2];
; #pragma unroll
;                     for (int bj = 0; bj < 2; ++bj) { const f32x4 v0 = acc[ai][bj][m][0] * W8_INV, v1 = acc[ai][bj][m][1] * W8_INV; o[bj].x = pk4_fp8(v0[0], v0[1], v0[2], v0[3]); o[bj].y = pk4_fp8(v1[0], v1[1], v1[2], v1[3]); }
;                     st_pair16(yp, 128, o[0], o[1], fq); } }
.LBB0_1644:
	s_mov_b64 s[98:99], s[46:47]
	v_mov_b32_e32 v11, v5
	v_mov_b32_e32 v6, v1
	v_readlane_b32 s6, v254, 36
	s_nop 15
	s_nop 15
	s_ashr_i32 s45, s44, 31
	v_readlane_b32 s9, v254, 38
	v_add_u32_e32 v24, s6, v6
	s_lshl_b32 s6, s44, 2
	s_add_i32 s6, s39, s6
	v_mov_b32_e32 v6, s6
	ds_read_b32 v6, v6
	v_cmp_gt_i32_e64 s[54:55], s93, v24
	s_waitcnt lgkmcnt(0)
	v_readfirstlane_b32 s6, v6
	s_sub_i32 s8, s42, s6
	s_lshl_b64 s[6:7], s[44:45], 18
	s_add_u32 s9, s9, s6
	v_readlane_b32 s6, v254, 34
	s_addc_u32 s10, s6, s7
	s_lshl_b32 s6, s8, 8
	s_ashr_i32 s7, s6, 31
	v_add_u32_e32 v6, 16, v24
	s_lshl_b64 s[6:7], s[6:7], 2
	v_cmp_gt_i32_e64 s[52:53], s93, v6
	s_add_u32 s30, s9, s6
	s_addc_u32 s31, s10, s7
	v_cndmask_b32_e64 v6, 0, v6, s[52:53]
	v_ashrrev_i32_e32 v7, 31, v6
	v_lshl_add_u64 v[6:7], v[6:7], 2, s[30:31]
	v_mov_b32_e32 v22, v206
	v_add_u32_e32 v6, 32, v24
	v_cmp_gt_i32_e64 s[50:51], s93, v6
	s_lshl_b32 s6, s66, 8
	s_or_b32 s6, s6, s95
	v_cndmask_b32_e64 v6, 0, v6, s[50:51]
	v_ashrrev_i32_e32 v7, 31, v6
	v_lshl_add_u64 v[6:7], v[6:7], 2, s[30:31]
	v_mov_b32_e32 v20, v235
	v_add_u32_e32 v6, 48, v24
	v_cmp_gt_i32_e64 s[48:49], s93, v6
	v_lshl_add_u32 v8, v11, 3, s6
	v_ashrrev_i32_e32 v9, 31, v8
	v_cndmask_b32_e64 v6, 0, v6, s[48:49]
	v_ashrrev_i32_e32 v7, 31, v6
	v_lshl_add_u64 v[6:7], v[6:7], 2, s[30:31]
	v_mov_b32_e32 v18, v244
	v_add_u32_e32 v6, 0x80, v24
	v_cmp_gt_i32_e64 s[46:47], s93, v6
	s_nop 1
	v_cndmask_b32_e64 v6, 0, v6, s[46:47]
	v_ashrrev_i32_e32 v7, 31, v6
	v_lshl_add_u64 v[6:7], v[6:7], 2, s[30:31]
	v_mov_b32_e32 v16, v245
	v_add_u32_e32 v6, 0x90, v24
	v_cmp_gt_i32_e64 s[44:45], s93, v6
	s_nop 1
	v_cndmask_b32_e64 v6, 0, v6, s[44:45]
	v_ashrrev_i32_e32 v7, 31, v6
	v_lshl_add_u64 v[6:7], v[6:7], 2, s[30:31]
	v_mov_b32_e32 v14, v246
	v_add_u32_e32 v6, 0xa0, v24
	v_cmp_gt_i32_e64 s[42:43], s93, v6
	s_nop 1
	v_cndmask_b32_e64 v6, 0, v6, s[42:43]
	v_ashrrev_i32_e32 v7, 31, v6
	v_lshl_add_u64 v[6:7], v[6:7], 2, s[30:31]
	v_mov_b32_e32 v12, v247
	v_add_u32_e32 v6, 0xb0, v24
	v_cmp_gt_i32_e32 vcc, s93, v6
	s_nop 1
	v_cndmask_b32_e32 v6, 0, v6, vcc
	v_ashrrev_i32_e32 v7, 31, v6
	v_lshl_add_u64 v[6:7], v[6:7], 2, s[30:31]
	v_mov_b32_e32 v10, v249
	v_bfe_i32 v6, v11, 0, 1
	v_and_b32_e32 v6, 0x78, v6
	v_mov_b32_e32 v7, v4
	v_mov_b32_e32 v25, v203
	s_cmp_eq_u64 s[98:99], 0
	s_cbranch_scc1 .Lm2_noslot
	s_lshl_b32 s98, s60, 2
	s_add_i32 s98, s39, s98
	v_mov_b32_e32 v203, s98
	ds_read_b32 v203, v203
	v_readlane_b32 s100, v254, 38
	v_readlane_b32 s101, v254, 34
	s_lshl_b32 s98, s60, 18
	s_add_u32 s100, s100, s98
	s_addc_u32 s101, s101, 0
	s_waitcnt lgkmcnt(0)
	v_readfirstlane_b32 s98, v203
	s_sub_i32 s98, s16, s98
	s_lshl_b32 s98, s98, 10
	s_ashr_i32 s99, s98, 31
	s_add_u32 s100, s100, s98
	s_addc_u32 s101, s101, s99
	v_readlane_b32 s98, v254, 36
	s_nop 1
	v_add_u32_e32 v203, s98, v1
	v_add_u32_e32 v206, 0x10, v203
	v_add_u32_e32 v235, 0x20, v203
	v_add_u32_e32 v244, 0x30, v203
	v_add_u32_e32 v245, 0x80, v203
	v_add_u32_e32 v246, 0x90, v203
	v_add_u32_e32 v247, 0xa0, v203
	v_add_u32_e32 v249, 0xb0, v203
	v_cmp_gt_i32_e64 s[98:99], s94, v206
	s_nop 1
	v_cndmask_b32_e64 v206, 0, v206, s[98:99]
	v_lshlrev_b32_e32 v206, 2, v206
	global_load_dword v206, v206, s[100:101]
	v_cmp_gt_i32_e64 s[98:99], s94, v235
	s_nop 1
	v_cndmask_b32_e64 v235, 0, v235, s[98:99]
	v_lshlrev_b32_e32 v235, 2, v235
	global_load_dword v235, v235, s[100:101]
	v_cmp_gt_i32_e64 s[98:99], s94, v244
	s_nop 1
	v_cndmask_b32_e64 v244, 0, v244, s[98:99]
	v_lshlrev_b32_e32 v244, 2, v244
	global_load_dword v244, v244, s[100:101]
	v_cmp_gt_i32_e64 s[98:99], s94, v245
	s_nop 1
	v_cndmask_b32_e64 v245, 0, v245, s[98:99]
	v_lshlrev_b32_e32 v245, 2, v245
	global_load_dword v245, v245, s[100:101]
	v_cmp_gt_i32_e64 s[98:99], s94, v246
	s_nop 1
	v_cndmask_b32_e64 v246, 0, v246, s[98:99]
	v_lshlrev_b32_e32 v246, 2, v246
	global_load_dword v246, v246, s[100:101]
	v_cmp_gt_i32_e64 s[98:99], s94, v247
	s_nop 1
	v_cndmask_b32_e64 v247, 0, v247, s[98:99]
	v_lshlrev_b32_e32 v247, 2, v247
	global_load_dword v247, v247, s[100:101]
	v_cmp_gt_i32_e64 s[98:99], s94, v249
	s_nop 1
	v_cndmask_b32_e64 v249, 0, v249, s[98:99]
	v_lshlrev_b32_e32 v249, 2, v249
	global_load_dword v249, v249, s[100:101]
	v_cmp_gt_i32_e64 s[98:99], s94, v203
	s_nop 1
	v_cndmask_b32_e64 v203, 0, v203, s[98:99]
	v_lshlrev_b32_e32 v203, 2, v203
	global_load_dword v203, v203, s[100:101]
.Lm2_noslot:
	s_and_saveexec_b64 s[66:67], s[54:55]
	s_cbranch_execz .LBB0_1653
	v_mov_b32_e32 v24, v25
	v_pk_mul_f32 v[26:27], v[164:165], s[34:35] op_sel_hi:[1,0]
	v_pk_mul_f32 v[32:33], v[158:159], s[34:35] op_sel_hi:[1,0]
	v_pk_mul_f32 v[30:31], v[160:161], s[34:35] op_sel_hi:[1,0]
	v_pk_mul_f32 v[34:35], v[150:151], s[34:35] op_sel_hi:[1,0]
	s_nop 0
	v_ashrrev_i32_e32 v25, 31, v24
	v_lshlrev_b64 v[24:25], 10, v[24:25]
	v_lshl_add_u64 v[28:29], s[56:57], 0, v[24:25]
	v_pk_mul_f32 v[24:25], v[162:163], s[34:35] op_sel_hi:[1,0]
	v_lshl_add_u64 v[28:29], v[28:29], 0, v[8:9]
	v_med3_f32 v11, v24, s35, v225
	v_med3_f32 v13, v25, s35, v225
	v_mov_b32_e32 v24, v4
	v_cvt_pk_fp8_f32 v24, v11, v13
	v_med3_f32 v11, v26, s35, v225
	v_med3_f32 v13, v27, s35, v225
	v_mov_b32_e32 v25, v4
	v_cvt_pk_fp8_f32 v24, v11, v13 op_sel:[0,0,1]
	v_med3_f32 v11, v32, s35, v225
	v_med3_f32 v13, v33, s35, v225
	v_cvt_pk_fp8_f32 v25, v11, v13
	v_med3_f32 v11, v30, s35, v225
	v_med3_f32 v13, v31, s35, v225
	v_pk_mul_f32 v[26:27], v[154:155], s[34:35] op_sel_hi:[1,0]
	v_cvt_pk_fp8_f32 v25, v11, v13 op_sel:[0,0,1]
	v_med3_f32 v11, v26, s35, v225
	v_med3_f32 v13, v27, s35, v225
	v_mov_b32_e32 v26, v4
	v_cvt_pk_fp8_f32 v26, v11, v13
	v_pk_mul_f32 v[30:31], v[156:157], s[34:35] op_sel_hi:[1,0]
	v_mov_b32_e32 v27, v4
	v_med3_f32 v11, v30, s35, v225
	v_med3_f32 v13, v31, s35, v225
	v_cvt_pk_fp8_f32 v26, v11, v13 op_sel:[0,0,1]
	v_med3_f32 v11, v34, s35, v225
	v_med3_f32 v13, v35, s35, v225
	v_cvt_pk_fp8_f32 v27, v11, v13
	v_pk_mul_f32 v[32:33], v[152:153], s[34:35] op_sel_hi:[1,0]
	v_permlane16_swap_b32_e32 v24, v26
	v_med3_f32 v11, v32, s35, v225
	v_med3_f32 v13, v33, s35, v225
	v_cvt_pk_fp8_f32 v27, v11, v13 op_sel:[0,0,1]
	v_lshl_add_u64 v[28:29], v[28:29], 0, v[6:7]
	s_nop 0
	v_permlane16_swap_b32_e32 v25, v27
	global_store_dwordx4 v[28:29], v[24:27], off
	s_or_b64 exec, exec, s[66:67]
	s_and_saveexec_b64 s[30:31], s[52:53]
	s_cbranch_execnz .LBB0_1654

; DI unsigned pk4_fp8(float a, float b, float c_, float d) { int w = 0; w = __builtin_amdgcn_cvt_pk_fp8_f32(clamp8(a), clamp8(b), w, false); w = __builtin_amdgcn_cvt_pk_fp8_f32(clamp8(c_), clamp8(d), w, true); return (unsigned)w; }
;     DI void operator()(const f32x4 (&acc)[2][2][4][2], const Unit& u, int wr, int wc, int fr, int fq) const {
;     ...
;             for (int m = 0; m < 4; ++m) { const int r = lrow0 + ai * 128 + m * 16;
;                 if (r < u.nv) { const int slot = slotv[ai * 4 + m]; unsigned char* yp = ys + (size_t)slot * 1024 + col0;
;                     u32x2 o[2];
; #pragma unroll
;                     for (int bj = 0; bj < 2; ++bj) { const f32x4 v0 = acc[ai][bj][m][0] * W8_INV, v1 = acc[ai][bj][m][1] * W8_INV; o[bj].x = pk4_fp8(v0[0], v0[1], v0[2], v0[3]); o[bj].y = pk4_fp8(v1[0], v1[1], v1[2], v1[3]); }
;                     st_pair16(yp, 128, o[0], o[1], fq); } }
.LBB0_1647:
	s_nop 0
	v_ashrrev_i32_e32 v21, 31, v20
	v_lshlrev_b64 v[20:21], 10, v[20:21]
	v_lshl_add_u64 v[24:25], s[56:57], 0, v[20:21]
	v_pk_mul_f32 v[20:21], v[130:131], s[34:35] op_sel_hi:[1,0]
	v_pk_mul_f32 v[28:29], v[126:127], s[34:35] op_sel_hi:[1,0]
	v_med3_f32 v11, v20, s35, v225
	v_med3_f32 v13, v21, s35, v225
	v_mov_b32_e32 v20, v4
	v_cvt_pk_fp8_f32 v20, v11, v13
	v_med3_f32 v15, v28, s35, v225
	v_med3_f32 v17, v29, s35, v225
	v_mov_b32_e32 v21, v4
	v_cvt_pk_fp8_f32 v21, v15, v17
	v_pk_mul_f32 v[22:23], v[132:133], s[34:35] op_sel_hi:[1,0]
	v_pk_mul_f32 v[26:27], v[128:129], s[34:35] op_sel_hi:[1,0]
	v_med3_f32 v11, v22, s35, v225
	v_med3_f32 v13, v23, s35, v225
	v_cvt_pk_fp8_f32 v20, v11, v13 op_sel:[0,0,1]
	v_med3_f32 v11, v26, s35, v225
	v_med3_f32 v13, v27, s35, v225
	v_pk_mul_f32 v[22:23], v[122:123], s[34:35] op_sel_hi:[1,0]
	v_cvt_pk_fp8_f32 v21, v11, v13 op_sel:[0,0,1]
	v_pk_mul_f32 v[30:31], v[118:119], s[34:35] op_sel_hi:[1,0]
	v_med3_f32 v11, v22, s35, v225
	v_med3_f32 v13, v23, s35, v225
	v_mov_b32_e32 v22, v4
	v_cvt_pk_fp8_f32 v22, v11, v13
	v_med3_f32 v15, v30, s35, v225
	v_med3_f32 v17, v31, s35, v225
	v_mov_b32_e32 v23, v4
	v_cvt_pk_fp8_f32 v23, v15, v17
	v_pk_mul_f32 v[26:27], v[124:125], s[34:35] op_sel_hi:[1,0]
	v_pk_mul_f32 v[28:29], v[120:121], s[34:35] op_sel_hi:[1,0]
	v_med3_f32 v11, v26, s35, v225
	v_med3_f32 v13, v27, s35, v225
	v_cvt_pk_fp8_f32 v22, v11, v13 op_sel:[0,0,1]
	v_med3_f32 v11, v28, s35, v225
	v_med3_f32 v13, v29, s35, v225
	v_cvt_pk_fp8_f32 v23, v11, v13 op_sel:[0,0,1]
	v_lshl_add_u64 v[24:25], v[24:25], 0, v[8:9]
	v_permlane16_swap_b32_e32 v20, v22
	v_permlane16_swap_b32_e32 v21, v23
	v_lshl_add_u64 v[24:25], v[24:25], 0, v[6:7]
	global_store_dwordx4 v[24:25], v[20:23], off
	s_or_b64 exec, exec, s[30:31]
	s_and_saveexec_b64 s[30:31], s[48:49]
	s_cbranch_execnz .LBB0_1656

; DI unsigned pk4_fp8(float a, float b, float c_, float d) { int w = 0; w = __builtin_amdgcn_cvt_pk_fp8_f32(clamp8(a), clamp8(b), w, false); w = __builtin_amdgcn_cvt_pk_fp8_f32(clamp8(c_), clamp8(d), w, true); return (unsigned)w; }
;     DI void operator()(const f32x4 (&acc)[2][2][4][2], const Unit& u, int wr, int wc, int fr, int fq) const {
;     ...
;             for (int m = 0; m < 4; ++m) { const int r = lrow0 + ai * 128 + m * 16;
;                 if (r < u.nv) { const int slot = slotv[ai * 4 + m]; unsigned char* yp = ys + (size_t)slot * 1024 + col0;
;                     u32x2 o[2];
; #pragma unroll
;                     for (int bj = 0; bj < 2; ++bj) { const f32x4 v0 = acc[ai][bj][m][0] * W8_INV, v1 = acc[ai][bj][m][1] * W8_INV; o[bj].x = pk4_fp8(v0[0], v0[1], v0[2], v0[3]); o[bj].y = pk4_fp8(v1[0], v1[1], v1[2], v1[3]); }
;                     st_pair16(yp, 128, o[0], o[1], fq); } }
.LBB0_1649:
	s_nop 0
	v_ashrrev_i32_e32 v17, 31, v16
	v_lshlrev_b64 v[16:17], 10, v[16:17]
	v_lshl_add_u64 v[20:21], s[56:57], 0, v[16:17]
	v_pk_mul_f32 v[16:17], v[114:115], s[34:35] op_sel_hi:[1,0]
	v_pk_mul_f32 v[18:19], v[116:117], s[34:35] op_sel_hi:[1,0]
	v_pk_mul_f32 v[24:25], v[110:111], s[34:35] op_sel_hi:[1,0]
	v_med3_f32 v11, v16, s35, v225
	v_med3_f32 v13, v17, s35, v225
	v_mov_b32_e32 v16, v4
	v_cvt_pk_fp8_f32 v16, v11, v13
	v_med3_f32 v11, v18, s35, v225
	v_med3_f32 v15, v24, s35, v225
	v_med3_f32 v18, v25, s35, v225
	v_mov_b32_e32 v17, v4
	v_cvt_pk_fp8_f32 v17, v15, v18
	v_pk_mul_f32 v[22:23], v[112:113], s[34:35] op_sel_hi:[1,0]
	v_med3_f32 v13, v19, s35, v225
	v_cvt_pk_fp8_f32 v16, v11, v13 op_sel:[0,0,1]
	v_med3_f32 v11, v22, s35, v225
	v_med3_f32 v13, v23, s35, v225
	v_pk_mul_f32 v[18:19], v[102:103], s[34:35] op_sel_hi:[1,0]
	v_cvt_pk_fp8_f32 v17, v11, v13 op_sel:[0,0,1]
	v_pk_mul_f32 v[22:23], v[104:105], s[34:35] op_sel_hi:[1,0]
	v_pk_mul_f32 v[26:27], v[94:95], s[34:35] op_sel_hi:[1,0]
	v_med3_f32 v11, v18, s35, v225
	v_med3_f32 v13, v19, s35, v225
	v_mov_b32_e32 v18, v4
	v_cvt_pk_fp8_f32 v18, v11, v13
	v_med3_f32 v11, v22, s35, v225
	v_med3_f32 v15, v26, s35, v225
	v_med3_f32 v22, v27, s35, v225
	v_mov_b32_e32 v19, v4
	v_cvt_pk_fp8_f32 v19, v15, v22
	v_pk_mul_f32 v[24:25], v[96:97], s[34:35] op_sel_hi:[1,0]
	v_med3_f32 v13, v23, s35, v225
	v_cvt_pk_fp8_f32 v18, v11, v13 op_sel:[0,0,1]
	v_med3_f32 v11, v24, s35, v225
	v_med3_f32 v13, v25, s35, v225
	v_cvt_pk_fp8_f32 v19, v11, v13 op_sel:[0,0,1]
	v_lshl_add_u64 v[20:21], v[20:21], 0, v[8:9]
	v_permlane16_swap_b32_e32 v16, v18
	v_permlane16_swap_b32_e32 v17, v19
	v_lshl_add_u64 v[20:21], v[20:21], 0, v[6:7]
	global_store_dwordx4 v[20:21], v[16:19], off
	s_or_b64 exec, exec, s[30:31]
	s_and_saveexec_b64 s[30:31], s[44:45]
	s_cbranch_execnz .LBB0_1658

; DI unsigned pk4_fp8(float a, float b, float c_, float d) { int w = 0; w = __builtin_amdgcn_cvt_pk_fp8_f32(clamp8(a), clamp8(b), w, false); w = __builtin_amdgcn_cvt_pk_fp8_f32(clamp8(c_), clamp8(d), w, true); return (unsigned)w; }
;     DI void operator()(const f32x4 (&acc)[2][2][4][2], const Unit& u, int wr, int wc, int fr, int fq) const {
;     ...
;             for (int m = 0; m < 4; ++m) { const int r = lrow0 + ai * 128 + m * 16;
;                 if (r < u.nv) { const int slot = slotv[ai * 4 + m]; unsigned char* yp = ys + (size_t)slot * 1024 + col0;
;                     u32x2 o[2];
; #pragma unroll
;                     for (int bj = 0; bj < 2; ++bj) { const f32x4 v0 = acc[ai][bj][m][0] * W8_INV, v1 = acc[ai][bj][m][1] * W8_INV; o[bj].x = pk4_fp8(v0[0], v0[1], v0[2], v0[3]); o[bj].y = pk4_fp8(v1[0], v1[1], v1[2], v1[3]); }
;                     st_pair16(yp, 128, o[0], o[1], fq); } }
.LBB0_1651:
	s_nop 0
	v_ashrrev_i32_e32 v13, 31, v12
	v_lshlrev_b64 v[12:13], 10, v[12:13]
	v_lshl_add_u64 v[16:17], s[56:57], 0, v[12:13]
	v_pk_mul_f32 v[12:13], v[66:67], s[34:35] op_sel_hi:[1,0]
	v_pk_mul_f32 v[14:15], v[68:69], s[34:35] op_sel_hi:[1,0]
	v_pk_mul_f32 v[20:21], v[62:63], s[34:35] op_sel_hi:[1,0]
	v_med3_f32 v11, v12, s35, v225
	v_med3_f32 v13, v13, s35, v225
	v_mov_b32_e32 v12, v4
	v_cvt_pk_fp8_f32 v12, v11, v13
	v_med3_f32 v11, v14, s35, v225
	v_med3_f32 v14, v15, s35, v225
	v_med3_f32 v15, v20, s35, v225
	v_med3_f32 v20, v21, s35, v225
	v_mov_b32_e32 v13, v4
	v_cvt_pk_fp8_f32 v13, v15, v20
	v_pk_mul_f32 v[18:19], v[64:65], s[34:35] op_sel_hi:[1,0]
	v_cvt_pk_fp8_f32 v12, v11, v14 op_sel:[0,0,1]
	v_med3_f32 v11, v18, s35, v225
	v_med3_f32 v14, v19, s35, v225
	v_cvt_pk_fp8_f32 v13, v11, v14 op_sel:[0,0,1]
	v_pk_mul_f32 v[14:15], v[58:59], s[34:35] op_sel_hi:[1,0]
	v_pk_mul_f32 v[18:19], v[60:61], s[34:35] op_sel_hi:[1,0]
	v_pk_mul_f32 v[22:23], v[54:55], s[34:35] op_sel_hi:[1,0]
	v_med3_f32 v11, v14, s35, v225
	v_med3_f32 v15, v15, s35, v225
	v_mov_b32_e32 v14, v4
	v_cvt_pk_fp8_f32 v14, v11, v15
	v_med3_f32 v11, v18, s35, v225
	v_med3_f32 v18, v19, s35, v225
	v_med3_f32 v19, v22, s35, v225
	v_med3_f32 v22, v23, s35, v225
	v_mov_b32_e32 v15, v4
	v_cvt_pk_fp8_f32 v15, v19, v22
	v_pk_mul_f32 v[20:21], v[56:57], s[34:35] op_sel_hi:[1,0]
	v_cvt_pk_fp8_f32 v14, v11, v18 op_sel:[0,0,1]
	v_med3_f32 v11, v20, s35, v225
	v_med3_f32 v18, v21, s35, v225
	v_cvt_pk_fp8_f32 v15, v11, v18 op_sel:[0,0,1]
	v_lshl_add_u64 v[16:17], v[16:17], 0, v[8:9]
	v_permlane16_swap_b32_e32 v12, v14
	v_permlane16_swap_b32_e32 v13, v15
	v_lshl_add_u64 v[16:17], v[16:17], 0, v[6:7]
	global_store_dwordx4 v[16:17], v[12:15], off
	s_or_b64 exec, exec, s[30:31]
	s_and_saveexec_b64 s[30:31], vcc
	s_cbranch_execnz .LBB0_1660

; DI unsigned pk4_fp8(float a, float b, float c_, float d) { int w = 0; w = __builtin_amdgcn_cvt_pk_fp8_f32(clamp8(a), clamp8(b), w, false); w = __builtin_amdgcn_cvt_pk_fp8_f32(clamp8(c_), clamp8(d), w, true); return (unsigned)w; }
;     DI void operator()(const f32x4 (&acc)[2][2][4][2], const Unit& u, int wr, int wc, int fr, int fq) const {
;     ...
;             for (int m = 0; m < 4; ++m) { const int r = lrow0 + ai * 128 + m * 16;
;                 if (r < u.nv) { const int slot = slotv[ai * 4 + m]; unsigned char* yp = ys + (size_t)slot * 1024 + col0;
;                     u32x2 o[2];
; #pragma unroll
;                     for (int bj = 0; bj < 2; ++bj) { const f32x4 v0 = acc[ai][bj][m][0] * W8_INV, v1 = acc[ai][bj][m][1] * W8_INV; o[bj].x = pk4_fp8(v0[0], v0[1], v0[2], v0[3]); o[bj].y = pk4_fp8(v1[0], v1[1], v1[2], v1[3]); }
;                     st_pair16(yp, 128, o[0], o[1], fq); } }
.LBB0_1654:
	s_nop 0
	v_ashrrev_i32_e32 v23, 31, v22
	v_lshlrev_b64 v[22:23], 10, v[22:23]
	v_lshl_add_u64 v[26:27], s[56:57], 0, v[22:23]
	v_pk_mul_f32 v[22:23], v[146:147], s[34:35] op_sel_hi:[1,0]
	v_pk_mul_f32 v[30:31], v[142:143], s[34:35] op_sel_hi:[1,0]
	v_med3_f32 v11, v22, s35, v225
	v_med3_f32 v13, v23, s35, v225
	v_mov_b32_e32 v22, v4
	v_cvt_pk_fp8_f32 v22, v11, v13
	v_med3_f32 v15, v30, s35, v225
	v_med3_f32 v17, v31, s35, v225
	v_mov_b32_e32 v23, v4
	v_cvt_pk_fp8_f32 v23, v15, v17
	v_pk_mul_f32 v[24:25], v[148:149], s[34:35] op_sel_hi:[1,0]
	v_pk_mul_f32 v[28:29], v[144:145], s[34:35] op_sel_hi:[1,0]
	v_med3_f32 v11, v24, s35, v225
	v_med3_f32 v13, v25, s35, v225
	v_cvt_pk_fp8_f32 v22, v11, v13 op_sel:[0,0,1]
	v_med3_f32 v11, v28, s35, v225
	v_med3_f32 v13, v29, s35, v225
	v_pk_mul_f32 v[24:25], v[138:139], s[34:35] op_sel_hi:[1,0]
	v_cvt_pk_fp8_f32 v23, v11, v13 op_sel:[0,0,1]
	v_pk_mul_f32 v[32:33], v[134:135], s[34:35] op_sel_hi:[1,0]
	v_med3_f32 v11, v24, s35, v225
	v_med3_f32 v13, v25, s35, v225
	v_mov_b32_e32 v24, v4
	v_cvt_pk_fp8_f32 v24, v11, v13
	v_med3_f32 v15, v32, s35, v225
	v_med3_f32 v17, v33, s35, v225
	v_mov_b32_e32 v25, v4
	v_cvt_pk_fp8_f32 v25, v15, v17
	v_pk_mul_f32 v[28:29], v[140:141], s[34:35] op_sel_hi:[1,0]
	v_pk_mul_f32 v[30:31], v[136:137], s[34:35] op_sel_hi:[1,0]
	v_med3_f32 v11, v28, s35, v225
	v_med3_f32 v13, v29, s35, v225
	v_cvt_pk_fp8_f32 v24, v11, v13 op_sel:[0,0,1]
	v_med3_f32 v11, v30, s35, v225
	v_med3_f32 v13, v31, s35, v225
	v_cvt_pk_fp8_f32 v25, v11, v13 op_sel:[0,0,1]
	v_lshl_add_u64 v[26:27], v[26:27], 0, v[8:9]
	v_permlane16_swap_b32_e32 v22, v24
	v_permlane16_swap_b32_e32 v23, v25
	v_lshl_add_u64 v[26:27], v[26:27], 0, v[6:7]
	global_store_dwordx4 v[26:27], v[22:25], off
	s_or_b64 exec, exec, s[30:31]
	s_and_saveexec_b64 s[30:31], s[50:51]
	s_cbranch_execnz .LBB0_1647

; DI unsigned pk4_fp8(float a, float b, float c_, float d) { int w = 0; w = __builtin_amdgcn_cvt_pk_fp8_f32(clamp8(a), clamp8(b), w, false); w = __builtin_amdgcn_cvt_pk_fp8_f32(clamp8(c_), clamp8(d), w, true); return (unsigned)w; }
;     DI void operator()(const f32x4 (&acc)[2][2][4][2], const Unit& u, int wr, int wc, int fr, int fq) const {
;     ...
;             for (int m = 0; m < 4; ++m) { const int r = lrow0 + ai * 128 + m * 16;
;                 if (r < u.nv) { const int slot = slotv[ai * 4 + m]; unsigned char* yp = ys + (size_t)slot * 1024 + col0;
;                     u32x2 o[2];
; #pragma unroll
;                     for (int bj = 0; bj < 2; ++bj) { const f32x4 v0 = acc[ai][bj][m][0] * W8_INV, v1 = acc[ai][bj][m][1] * W8_INV; o[bj].x = pk4_fp8(v0[0], v0[1], v0[2], v0[3]); o[bj].y = pk4_fp8(v1[0], v1[1], v1[2], v1[3]); }
;                     st_pair16(yp, 128, o[0], o[1], fq); } }
.LBB0_1656:
	s_nop 0
	v_ashrrev_i32_e32 v19, 31, v18
	v_lshlrev_b64 v[18:19], 10, v[18:19]
	v_lshl_add_u64 v[22:23], s[56:57], 0, v[18:19]
	v_pk_mul_f32 v[18:19], v[106:107], s[34:35] op_sel_hi:[1,0]
	v_pk_mul_f32 v[26:27], v[98:99], s[34:35] op_sel_hi:[1,0]
	v_med3_f32 v11, v18, s35, v225
	v_med3_f32 v13, v19, s35, v225
	v_mov_b32_e32 v18, v4
	v_cvt_pk_fp8_f32 v18, v11, v13
	v_med3_f32 v15, v26, s35, v225
	v_med3_f32 v17, v27, s35, v225
	v_mov_b32_e32 v19, v4
	v_cvt_pk_fp8_f32 v19, v15, v17
	v_pk_mul_f32 v[20:21], v[108:109], s[34:35] op_sel_hi:[1,0]
	v_pk_mul_f32 v[24:25], v[100:101], s[34:35] op_sel_hi:[1,0]
	v_med3_f32 v11, v20, s35, v225
	v_med3_f32 v13, v21, s35, v225
	v_cvt_pk_fp8_f32 v18, v11, v13 op_sel:[0,0,1]
	v_med3_f32 v11, v24, s35, v225
	v_med3_f32 v13, v25, s35, v225
	v_pk_mul_f32 v[20:21], v[90:91], s[34:35] op_sel_hi:[1,0]
	v_cvt_pk_fp8_f32 v19, v11, v13 op_sel:[0,0,1]
	v_pk_mul_f32 v[28:29], v[86:87], s[34:35] op_sel_hi:[1,0]
	v_med3_f32 v11, v20, s35, v225
	v_med3_f32 v13, v21, s35, v225
	v_mov_b32_e32 v20, v4
	v_cvt_pk_fp8_f32 v20, v11, v13
	v_med3_f32 v15, v28, s35, v225
	v_med3_f32 v17, v29, s35, v225
	v_mov_b32_e32 v21, v4
	v_cvt_pk_fp8_f32 v21, v15, v17
	v_pk_mul_f32 v[24:25], v[92:93], s[34:35] op_sel_hi:[1,0]
	v_pk_mul_f32 v[26:27], v[88:89], s[34:35] op_sel_hi:[1,0]
	v_med3_f32 v11, v24, s35, v225
	v_med3_f32 v13, v25, s35, v225
	v_cvt_pk_fp8_f32 v20, v11, v13 op_sel:[0,0,1]
	v_med3_f32 v11, v26, s35, v225
	v_med3_f32 v13, v27, s35, v225
	v_cvt_pk_fp8_f32 v21, v11, v13 op_sel:[0,0,1]
	v_lshl_add_u64 v[22:23], v[22:23], 0, v[8:9]
	v_permlane16_swap_b32_e32 v18, v20
	v_permlane16_swap_b32_e32 v19, v21
	v_lshl_add_u64 v[22:23], v[22:23], 0, v[6:7]
	global_store_dwordx4 v[22:23], v[18:21], off
	s_or_b64 exec, exec, s[30:31]
	s_and_saveexec_b64 s[30:31], s[46:47]
	s_cbranch_execnz .LBB0_1649

; DI unsigned pk4_fp8(float a, float b, float c_, float d) { int w = 0; w = __builtin_amdgcn_cvt_pk_fp8_f32(clamp8(a), clamp8(b), w, false); w = __builtin_amdgcn_cvt_pk_fp8_f32(clamp8(c_), clamp8(d), w, true); return (unsigned)w; }
;     DI void operator()(const f32x4 (&acc)[2][2][4][2], const Unit& u, int wr, int wc, int fr, int fq) const {
;     ...
;             for (int m = 0; m < 4; ++m) { const int r = lrow0 + ai * 128 + m * 16;
;                 if (r < u.nv) { const int slot = slotv[ai * 4 + m]; unsigned char* yp = ys + (size_t)slot * 1024 + col0;
;                     u32x2 o[2];
; #pragma unroll
;                     for (int bj = 0; bj < 2; ++bj) { const f32x4 v0 = acc[ai][bj][m][0] * W8_INV, v1 = acc[ai][bj][m][1] * W8_INV; o[bj].x = pk4_fp8(v0[0], v0[1], v0[2], v0[3]); o[bj].y = pk4_fp8(v1[0], v1[1], v1[2], v1[3]); }
;                     st_pair16(yp, 128, o[0], o[1], fq); } }
.LBB0_1658:
	s_nop 0
	v_ashrrev_i32_e32 v15, 31, v14
	v_lshlrev_b64 v[14:15], 10, v[14:15]
	v_lshl_add_u64 v[18:19], s[56:57], 0, v[14:15]
	v_pk_mul_f32 v[14:15], v[82:83], s[34:35] op_sel_hi:[1,0]
	v_pk_mul_f32 v[16:17], v[84:85], s[34:35] op_sel_hi:[1,0]
	v_pk_mul_f32 v[22:23], v[78:79], s[34:35] op_sel_hi:[1,0]
	v_med3_f32 v11, v14, s35, v225
	v_med3_f32 v13, v15, s35, v225
	v_mov_b32_e32 v14, v4
	v_cvt_pk_fp8_f32 v14, v11, v13
	v_med3_f32 v11, v16, s35, v225
	v_med3_f32 v13, v17, s35, v225
	v_med3_f32 v16, v22, s35, v225
	v_med3_f32 v17, v23, s35, v225
	v_mov_b32_e32 v15, v4
	v_cvt_pk_fp8_f32 v15, v16, v17
	v_pk_mul_f32 v[20:21], v[80:81], s[34:35] op_sel_hi:[1,0]
	v_cvt_pk_fp8_f32 v14, v11, v13 op_sel:[0,0,1]
	v_med3_f32 v11, v20, s35, v225
	v_med3_f32 v13, v21, s35, v225
	v_pk_mul_f32 v[16:17], v[74:75], s[34:35] op_sel_hi:[1,0]
	v_cvt_pk_fp8_f32 v15, v11, v13 op_sel:[0,0,1]
	v_pk_mul_f32 v[20:21], v[76:77], s[34:35] op_sel_hi:[1,0]
	v_pk_mul_f32 v[24:25], v[70:71], s[34:35] op_sel_hi:[1,0]
	v_med3_f32 v11, v16, s35, v225
	v_med3_f32 v13, v17, s35, v225
	v_mov_b32_e32 v16, v4
	v_cvt_pk_fp8_f32 v16, v11, v13
	v_med3_f32 v11, v20, s35, v225
	v_med3_f32 v13, v21, s35, v225
	v_med3_f32 v20, v24, s35, v225
	v_med3_f32 v21, v25, s35, v225
	v_mov_b32_e32 v17, v4
	v_cvt_pk_fp8_f32 v17, v20, v21
	v_pk_mul_f32 v[22:23], v[72:73], s[34:35] op_sel_hi:[1,0]
	v_cvt_pk_fp8_f32 v16, v11, v13 op_sel:[0,0,1]
	v_med3_f32 v11, v22, s35, v225
	v_med3_f32 v13, v23, s35, v225
	v_cvt_pk_fp8_f32 v17, v11, v13 op_sel:[0,0,1]
	v_lshl_add_u64 v[18:19], v[18:19], 0, v[8:9]
	v_permlane16_swap_b32_e32 v14, v16
	v_permlane16_swap_b32_e32 v15, v17
	v_lshl_add_u64 v[18:19], v[18:19], 0, v[6:7]
	global_store_dwordx4 v[18:19], v[14:17], off
	s_or_b64 exec, exec, s[30:31]
	s_and_saveexec_b64 s[30:31], s[42:43]
	s_cbranch_execnz .LBB0_1651

; DI unsigned pk4_fp8(float a, float b, float c_, float d) { int w = 0; w = __builtin_amdgcn_cvt_pk_fp8_f32(clamp8(a), clamp8(b), w, false); w = __builtin_amdgcn_cvt_pk_fp8_f32(clamp8(c_), clamp8(d), w, true); return (unsigned)w; }
;     DI void operator()(const f32x4 (&acc)[2][2][4][2], const Unit& u, int wr, int wc, int fr, int fq) const {
;     ...
;             for (int m = 0; m < 4; ++m) { const int r = lrow0 + ai * 128 + m * 16;
;                 if (r < u.nv) { const int slot = slotv[ai * 4 + m]; unsigned char* yp = ys + (size_t)slot * 1024 + col0;
;                     u32x2 o[2];
; #pragma unroll
;                     for (int bj = 0; bj < 2; ++bj) { const f32x4 v0 = acc[ai][bj][m][0] * W8_INV, v1 = acc[ai][bj][m][1] * W8_INV; o[bj].x = pk4_fp8(v0[0], v0[1], v0[2], v0[3]); o[bj].y = pk4_fp8(v1[0], v1[1], v1[2], v1[3]); }
;                     st_pair16(yp, 128, o[0], o[1], fq); } }
.LBB0_1660:
	s_nop 0
	v_ashrrev_i32_e32 v11, 31, v10
	v_lshlrev_b64 v[10:11], 10, v[10:11]
	v_lshl_add_u64 v[14:15], s[56:57], 0, v[10:11]
	v_pk_mul_f32 v[10:11], v[50:51], s[34:35] op_sel_hi:[1,0]
	v_pk_mul_f32 v[18:19], v[46:47], s[34:35] op_sel_hi:[1,0]
	v_med3_f32 v20, v10, s35, v225
	v_med3_f32 v11, v11, s35, v225
	v_mov_b32_e32 v10, v4
	v_cvt_pk_fp8_f32 v10, v20, v11
	v_med3_f32 v18, v18, s35, v225
	v_med3_f32 v19, v19, s35, v225
	v_mov_b32_e32 v11, v4
	v_cvt_pk_fp8_f32 v11, v18, v19
	v_pk_mul_f32 v[12:13], v[52:53], s[34:35] op_sel_hi:[1,0]
	v_pk_mul_f32 v[16:17], v[48:49], s[34:35] op_sel_hi:[1,0]
	v_med3_f32 v12, v12, s35, v225
	v_med3_f32 v13, v13, s35, v225
	v_cvt_pk_fp8_f32 v10, v12, v13 op_sel:[0,0,1]
	v_med3_f32 v12, v16, s35, v225
	v_med3_f32 v13, v17, s35, v225
	v_cvt_pk_fp8_f32 v11, v12, v13 op_sel:[0,0,1]
	v_pk_mul_f32 v[12:13], v[42:43], s[34:35] op_sel_hi:[1,0]
	v_pk_mul_f32 v[20:21], v[38:39], s[34:35] op_sel_hi:[1,0]
	v_med3_f32 v22, v12, s35, v225
	v_med3_f32 v13, v13, s35, v225
	v_mov_b32_e32 v12, v4
	v_cvt_pk_fp8_f32 v12, v22, v13
	v_med3_f32 v20, v20, s35, v225
	v_med3_f32 v21, v21, s35, v225
	v_mov_b32_e32 v13, v4
	v_cvt_pk_fp8_f32 v13, v20, v21
	v_pk_mul_f32 v[16:17], v[44:45], s[34:35] op_sel_hi:[1,0]
	v_pk_mul_f32 v[18:19], v[40:41], s[34:35] op_sel_hi:[1,0]
	v_med3_f32 v16, v16, s35, v225
	v_med3_f32 v17, v17, s35, v225
	v_cvt_pk_fp8_f32 v12, v16, v17 op_sel:[0,0,1]
	v_med3_f32 v16, v18, s35, v225
	v_med3_f32 v17, v19, s35, v225
	v_cvt_pk_fp8_f32 v13, v16, v17 op_sel:[0,0,1]
	v_lshl_add_u64 v[8:9], v[14:15], 0, v[8:9]
	v_permlane16_swap_b32_e32 v10, v12
	v_permlane16_swap_b32_e32 v11, v13
	v_lshl_add_u64 v[6:7], v[8:9], 0, v[6:7]
	global_store_dwordx4 v[6:7], v[10:13], off
	s_or_b64 exec, exec, s[30:31]
	s_and_b64 vcc, exec, s[40:41]
	s_mov_b64 s[30:31], -1
	s_cbranch_vccnz .LBB0_1635
